# adds: hyena implicit-filter third layer hand-written (plain f32 FMAs, weight loads one step ahead, LDS reads two positions ahead)
# speedup vs baseline: 1.0077x; 1.0077x over previous
;     ...
;     float asum = 0.f;
; #pragma unroll 1
;     for (int hp = 0; hp < 2; ++hp) {
;         float accf[16], accb[16];
; #pragma unroll
;         for (int i = 0; i < 16; ++i) { accf[i] = 0.f; accb[i] = 0.f; }
; #pragma unroll 2
;         for (int k4 = 0; k4 < 16; ++k4) {
;             float wf[4], wb[4];
; #pragma unroll
;             for (int j = 0; j < 4; ++j) { wf[j] = w3[(k4 * 4 + j) * 1024 + tid]; wb[j] = w3[(k4 * 4 + j) * 1024 + 512 + tid]; }
; #pragma unroll
;             for (int pp = 0; pp < 16; ++pp) {
;                 const float4 hv = *(const float4*)&h2[(hp * 16 + pp) * 64 + k4 * 4];
;                 accf[pp] += hv.x * wf[0]; accf[pp] += hv.y * wf[1]; accf[pp] += hv.z * wf[2]; accf[pp] += hv.w * wf[3];
;                 accb[pp] += hv.x * wb[0]; accb[pp] += hv.y * wb[1]; accb[pp] += hv.z * wb[2]; accb[pp] += hv.w * wb[3];
;             }
;         }
.LBB0_76:
	v_lshlrev_b32_e32 v62, 2, v0
	v_readlane_b32 s98, v253, 59
	v_readlane_b32 s99, v253, 60
	s_mov_b32 s101, s2
	s_mov_b32 s100, 0
	global_load_dword v78, v62, s[98:99]
	global_load_dword v82, v62, s[98:99] offset:2048
	s_add_u32 s98, s98, 0x1000
	s_addc_u32 s99, s99, 0
	global_load_dword v79, v62, s[98:99]
	global_load_dword v83, v62, s[98:99] offset:2048
	s_add_u32 s98, s98, 0x1000
	s_addc_u32 s99, s99, 0
	global_load_dword v80, v62, s[98:99]
	global_load_dword v84, v62, s[98:99] offset:2048
	s_add_u32 s98, s98, 0x1000
	s_addc_u32 s99, s99, 0
	global_load_dword v81, v62, s[98:99]
	global_load_dword v85, v62, s[98:99] offset:2048
	s_add_u32 s98, s98, 0x1000
	s_addc_u32 s99, s99, 0
.Lhy_loop:
	global_load_dword v86, v62, s[98:99]
	global_load_dword v90, v62, s[98:99] offset:2048
	s_add_u32 s98, s98, 0x1000
	s_addc_u32 s99, s99, 0
	global_load_dword v87, v62, s[98:99]
	global_load_dword v91, v62, s[98:99] offset:2048
	s_add_u32 s98, s98, 0x1000
	s_addc_u32 s99, s99, 0
	global_load_dword v88, v62, s[98:99]
	global_load_dword v92, v62, s[98:99] offset:2048
	s_add_u32 s98, s98, 0x1000
	s_addc_u32 s99, s99, 0
	global_load_dword v89, v62, s[98:99]
	global_load_dword v93, v62, s[98:99] offset:2048
	s_add_u32 s98, s98, 0x1000
	s_addc_u32 s99, s99, 0
	v_mov_b32_e32 v63, s101
	s_add_i32 s101, s101, 16
	ds_read_b128 v[94:97], v63
	ds_read_b128 v[98:101], v63 offset:256
	s_waitcnt vmcnt(8)
	ds_read_b128 v[58:61], v63 offset:512
	s_waitcnt lgkmcnt(2)
	v_fmac_f32_e32 v54, v78, v94
	v_fmac_f32_e32 v56, v82, v94
	v_fmac_f32_e32 v54, v79, v95
	v_fmac_f32_e32 v56, v83, v95
	v_fmac_f32_e32 v54, v80, v96
	v_fmac_f32_e32 v56, v84, v96
	v_fmac_f32_e32 v54, v81, v97
	v_fmac_f32_e32 v56, v85, v97
	ds_read_b128 v[94:97], v63 offset:768
	s_waitcnt lgkmcnt(2)
	v_fmac_f32_e32 v55, v78, v98
	v_fmac_f32_e32 v57, v82, v98
	v_fmac_f32_e32 v55, v79, v99
	v_fmac_f32_e32 v57, v83, v99
	v_fmac_f32_e32 v55, v80, v100
	v_fmac_f32_e32 v57, v84, v100
	v_fmac_f32_e32 v55, v81, v101
	v_fmac_f32_e32 v57, v85, v101
	ds_read_b128 v[98:101], v63 offset:1024
	s_waitcnt lgkmcnt(2)
	v_fmac_f32_e32 v50, v78, v58
	v_fmac_f32_e32 v52, v82, v58
	v_fmac_f32_e32 v50, v79, v59
	v_fmac_f32_e32 v52, v83, v59
	v_fmac_f32_e32 v50, v80, v60
	v_fmac_f32_e32 v52, v84, v60
	v_fmac_f32_e32 v50, v81, v61
	v_fmac_f32_e32 v52, v85, v61
	ds_read_b128 v[58:61], v63 offset:1280
	s_waitcnt lgkmcnt(2)
	v_fmac_f32_e32 v51, v78, v94
	v_fmac_f32_e32 v53, v82, v94
	v_fmac_f32_e32 v51, v79, v95
	v_fmac_f32_e32 v53, v83, v95
	v_fmac_f32_e32 v51, v80, v96
	v_fmac_f32_e32 v53, v84, v96
	v_fmac_f32_e32 v51, v81, v97
	v_fmac_f32_e32 v53, v85, v97
	ds_read_b128 v[94:97], v63 offset:1536
	s_waitcnt lgkmcnt(2)
	v_fmac_f32_e32 v46, v78, v98
	v_fmac_f32_e32 v48, v82, v98
	v_fmac_f32_e32 v46, v79, v99
	v_fmac_f32_e32 v48, v83, v99
	v_fmac_f32_e32 v46, v80, v100
	v_fmac_f32_e32 v48, v84, v100
	v_fmac_f32_e32 v46, v81, v101
	v_fmac_f32_e32 v48, v85, v101
	ds_read_b128 v[98:101], v63 offset:1792
	s_waitcnt lgkmcnt(2)
	v_fmac_f32_e32 v47, v78, v58
	v_fmac_f32_e32 v49, v82, v58
	v_fmac_f32_e32 v47, v79, v59
	v_fmac_f32_e32 v49, v83, v59
	v_fmac_f32_e32 v47, v80, v60
	v_fmac_f32_e32 v49, v84, v60
	v_fmac_f32_e32 v47, v81, v61
	v_fmac_f32_e32 v49, v85, v61
	ds_read_b128 v[58:61], v63 offset:2048
	s_waitcnt lgkmcnt(2)
	v_fmac_f32_e32 v42, v78, v94
	v_fmac_f32_e32 v44, v82, v94
	v_fmac_f32_e32 v42, v79, v95
	v_fmac_f32_e32 v44, v83, v95
	v_fmac_f32_e32 v42, v80, v96
	v_fmac_f32_e32 v44, v84, v96
	v_fmac_f32_e32 v42, v81, v97
	v_fmac_f32_e32 v44, v85, v97
	ds_read_b128 v[94:97], v63 offset:2304
	s_waitcnt lgkmcnt(2)
	v_fmac_f32_e32 v43, v78, v98
	v_fmac_f32_e32 v45, v82, v98
	v_fmac_f32_e32 v43, v79, v99
	v_fmac_f32_e32 v45, v83, v99
	v_fmac_f32_e32 v43, v80, v100
	v_fmac_f32_e32 v45, v84, v100
	v_fmac_f32_e32 v43, v81, v101
	v_fmac_f32_e32 v45, v85, v101
	ds_read_b128 v[98:101], v63 offset:2560
	s_waitcnt lgkmcnt(2)
	v_fmac_f32_e32 v38, v78, v58
	v_fmac_f32_e32 v40, v82, v58
	v_fmac_f32_e32 v38, v79, v59
	v_fmac_f32_e32 v40, v83, v59
	v_fmac_f32_e32 v38, v80, v60
	v_fmac_f32_e32 v40, v84, v60
	v_fmac_f32_e32 v38, v81, v61
	v_fmac_f32_e32 v40, v85, v61
	ds_read_b128 v[58:61], v63 offset:2816
	s_waitcnt lgkmcnt(2)
	v_fmac_f32_e32 v39, v78, v94
	v_fmac_f32_e32 v41, v82, v94
	v_fmac_f32_e32 v39, v79, v95
	v_fmac_f32_e32 v41, v83, v95
	v_fmac_f32_e32 v39, v80, v96
	v_fmac_f32_e32 v41, v84, v96
	v_fmac_f32_e32 v39, v81, v97
	v_fmac_f32_e32 v41, v85, v97
	ds_read_b128 v[94:97], v63 offset:3072
	s_waitcnt lgkmcnt(2)
	v_fmac_f32_e32 v34, v78, v98
	v_fmac_f32_e32 v36, v82, v98
	v_fmac_f32_e32 v34, v79, v99
	v_fmac_f32_e32 v36, v83, v99
	v_fmac_f32_e32 v34, v80, v100
	v_fmac_f32_e32 v36, v84, v100
	v_fmac_f32_e32 v34, v81, v101
	v_fmac_f32_e32 v36, v85, v101
	ds_read_b128 v[98:101], v63 offset:3328
	s_waitcnt lgkmcnt(2)
	v_fmac_f32_e32 v35, v78, v58
	v_fmac_f32_e32 v37, v82, v58
	v_fmac_f32_e32 v35, v79, v59
	v_fmac_f32_e32 v37, v83, v59
	v_fmac_f32_e32 v35, v80, v60
	v_fmac_f32_e32 v37, v84, v60
	v_fmac_f32_e32 v35, v81, v61
	v_fmac_f32_e32 v37, v85, v61
	ds_read_b128 v[58:61], v63 offset:3584
	s_waitcnt lgkmcnt(2)
	v_fmac_f32_e32 v30, v78, v94
	v_fmac_f32_e32 v32, v82, v94
	v_fmac_f32_e32 v30, v79, v95
	v_fmac_f32_e32 v32, v83, v95
	v_fmac_f32_e32 v30, v80, v96
	v_fmac_f32_e32 v32, v84, v96
	v_fmac_f32_e32 v30, v81, v97
	v_fmac_f32_e32 v32, v85, v97
	ds_read_b128 v[94:97], v63 offset:3840
	s_waitcnt lgkmcnt(2)
	v_fmac_f32_e32 v31, v78, v98
	v_fmac_f32_e32 v33, v82, v98
	v_fmac_f32_e32 v31, v79, v99
	v_fmac_f32_e32 v33, v83, v99
	v_fmac_f32_e32 v31, v80, v100
	v_fmac_f32_e32 v33, v84, v100
	v_fmac_f32_e32 v31, v81, v101
	v_fmac_f32_e32 v33, v85, v101
	s_waitcnt lgkmcnt(1)
	v_fmac_f32_e32 v26, v78, v58
	v_fmac_f32_e32 v28, v82, v58
	v_fmac_f32_e32 v26, v79, v59
	v_fmac_f32_e32 v28, v83, v59
	v_fmac_f32_e32 v26, v80, v60
	v_fmac_f32_e32 v28, v84, v60
	v_fmac_f32_e32 v26, v81, v61
	v_fmac_f32_e32 v28, v85, v61
	s_waitcnt lgkmcnt(0)
	v_fmac_f32_e32 v27, v78, v94
	v_fmac_f32_e32 v29, v82, v94
	v_fmac_f32_e32 v27, v79, v95
	v_fmac_f32_e32 v29, v83, v95
	v_fmac_f32_e32 v27, v80, v96
	v_fmac_f32_e32 v29, v84, v96
	v_fmac_f32_e32 v27, v81, v97
	v_fmac_f32_e32 v29, v85, v97
	s_cmp_eq_u32 s100, 7
	s_cbranch_scc1 .Lhy_last
;     ...
;         for (int k4 = 0; k4 < 16; ++k4) {
;             float wf[4], wb[4];
; #pragma unroll
;             for (int j = 0; j < 4; ++j) { wf[j] = w3[(k4 * 4 + j) * 1024 + tid]; wb[j] = w3[(k4 * 4 + j) * 1024 + 512 + tid]; }
; #pragma unroll
;             for (int pp = 0; pp < 16; ++pp) {
;                 const float4 hv = *(const float4*)&h2[(hp * 16 + pp) * 64 + k4 * 4];
;                 accf[pp] += hv.x * wf[0]; accf[pp] += hv.y * wf[1]; accf[pp] += hv.z * wf[2]; accf[pp] += hv.w * wf[3];
;                 accb[pp] += hv.x * wb[0]; accb[pp] += hv.y * wb[1]; accb[pp] += hv.z * wb[2]; accb[pp] += hv.w * wb[3];
;             }
;         }
	global_load_dword v78, v62, s[98:99]
	global_load_dword v82, v62, s[98:99] offset:2048
	s_add_u32 s98, s98, 0x1000
	s_addc_u32 s99, s99, 0
	global_load_dword v79, v62, s[98:99]
	global_load_dword v83, v62, s[98:99] offset:2048
	s_add_u32 s98, s98, 0x1000
	s_addc_u32 s99, s99, 0
	global_load_dword v80, v62, s[98:99]
	global_load_dword v84, v62, s[98:99] offset:2048
	s_add_u32 s98, s98, 0x1000
	s_addc_u32 s99, s99, 0
	global_load_dword v81, v62, s[98:99]
	global_load_dword v85, v62, s[98:99] offset:2048
	s_add_u32 s98, s98, 0x1000
	s_addc_u32 s99, s99, 0
	v_mov_b32_e32 v63, s101
	s_add_i32 s101, s101, 16
	ds_read_b128 v[94:97], v63
	ds_read_b128 v[98:101], v63 offset:256
	s_waitcnt vmcnt(8)
	ds_read_b128 v[58:61], v63 offset:512
	s_waitcnt lgkmcnt(2)
	v_fmac_f32_e32 v54, v86, v94
	v_fmac_f32_e32 v56, v90, v94
	v_fmac_f32_e32 v54, v87, v95
	v_fmac_f32_e32 v56, v91, v95
	v_fmac_f32_e32 v54, v88, v96
	v_fmac_f32_e32 v56, v92, v96
	v_fmac_f32_e32 v54, v89, v97
	v_fmac_f32_e32 v56, v93, v97
	ds_read_b128 v[94:97], v63 offset:768
	s_waitcnt lgkmcnt(2)
	v_fmac_f32_e32 v55, v86, v98
	v_fmac_f32_e32 v57, v90, v98
	v_fmac_f32_e32 v55, v87, v99
	v_fmac_f32_e32 v57, v91, v99
	v_fmac_f32_e32 v55, v88, v100
	v_fmac_f32_e32 v57, v92, v100
	v_fmac_f32_e32 v55, v89, v101
	v_fmac_f32_e32 v57, v93, v101
	ds_read_b128 v[98:101], v63 offset:1024
	s_waitcnt lgkmcnt(2)
	v_fmac_f32_e32 v50, v86, v58
	v_fmac_f32_e32 v52, v90, v58
	v_fmac_f32_e32 v50, v87, v59
	v_fmac_f32_e32 v52, v91, v59
	v_fmac_f32_e32 v50, v88, v60
	v_fmac_f32_e32 v52, v92, v60
	v_fmac_f32_e32 v50, v89, v61
	v_fmac_f32_e32 v52, v93, v61
	ds_read_b128 v[58:61], v63 offset:1280
	s_waitcnt lgkmcnt(2)
	v_fmac_f32_e32 v51, v86, v94
	v_fmac_f32_e32 v53, v90, v94
	v_fmac_f32_e32 v51, v87, v95
	v_fmac_f32_e32 v53, v91, v95
	v_fmac_f32_e32 v51, v88, v96
	v_fmac_f32_e32 v53, v92, v96
	v_fmac_f32_e32 v51, v89, v97
	v_fmac_f32_e32 v53, v93, v97
	ds_read_b128 v[94:97], v63 offset:1536
	s_waitcnt lgkmcnt(2)
	v_fmac_f32_e32 v46, v86, v98
	v_fmac_f32_e32 v48, v90, v98
	v_fmac_f32_e32 v46, v87, v99
	v_fmac_f32_e32 v48, v91, v99
	v_fmac_f32_e32 v46, v88, v100
	v_fmac_f32_e32 v48, v92, v100
	v_fmac_f32_e32 v46, v89, v101
	v_fmac_f32_e32 v48, v93, v101
	ds_read_b128 v[98:101], v63 offset:1792
	s_waitcnt lgkmcnt(2)
	v_fmac_f32_e32 v47, v86, v58
	v_fmac_f32_e32 v49, v90, v58
	v_fmac_f32_e32 v47, v87, v59
	v_fmac_f32_e32 v49, v91, v59
	v_fmac_f32_e32 v47, v88, v60
	v_fmac_f32_e32 v49, v92, v60
	v_fmac_f32_e32 v47, v89, v61
	v_fmac_f32_e32 v49, v93, v61
	ds_read_b128 v[58:61], v63 offset:2048
	s_waitcnt lgkmcnt(2)
	v_fmac_f32_e32 v42, v86, v94
	v_fmac_f32_e32 v44, v90, v94
	v_fmac_f32_e32 v42, v87, v95
	v_fmac_f32_e32 v44, v91, v95
	v_fmac_f32_e32 v42, v88, v96
	v_fmac_f32_e32 v44, v92, v96
	v_fmac_f32_e32 v42, v89, v97
	v_fmac_f32_e32 v44, v93, v97
	ds_read_b128 v[94:97], v63 offset:2304
	s_waitcnt lgkmcnt(2)
	v_fmac_f32_e32 v43, v86, v98
	v_fmac_f32_e32 v45, v90, v98
	v_fmac_f32_e32 v43, v87, v99
	v_fmac_f32_e32 v45, v91, v99
	v_fmac_f32_e32 v43, v88, v100
	v_fmac_f32_e32 v45, v92, v100
	v_fmac_f32_e32 v43, v89, v101
	v_fmac_f32_e32 v45, v93, v101
	ds_read_b128 v[98:101], v63 offset:2560
	s_waitcnt lgkmcnt(2)
	v_fmac_f32_e32 v38, v86, v58
	v_fmac_f32_e32 v40, v90, v58
	v_fmac_f32_e32 v38, v87, v59
	v_fmac_f32_e32 v40, v91, v59
	v_fmac_f32_e32 v38, v88, v60
	v_fmac_f32_e32 v40, v92, v60
	v_fmac_f32_e32 v38, v89, v61
	v_fmac_f32_e32 v40, v93, v61
	ds_read_b128 v[58:61], v63 offset:2816
	s_waitcnt lgkmcnt(2)
	v_fmac_f32_e32 v39, v86, v94
	v_fmac_f32_e32 v41, v90, v94
	v_fmac_f32_e32 v39, v87, v95
	v_fmac_f32_e32 v41, v91, v95
	v_fmac_f32_e32 v39, v88, v96
	v_fmac_f32_e32 v41, v92, v96
	v_fmac_f32_e32 v39, v89, v97
	v_fmac_f32_e32 v41, v93, v97
	ds_read_b128 v[94:97], v63 offset:3072
	s_waitcnt lgkmcnt(2)
	v_fmac_f32_e32 v34, v86, v98
	v_fmac_f32_e32 v36, v90, v98
	v_fmac_f32_e32 v34, v87, v99
	v_fmac_f32_e32 v36, v91, v99
	v_fmac_f32_e32 v34, v88, v100
	v_fmac_f32_e32 v36, v92, v100
	v_fmac_f32_e32 v34, v89, v101
	v_fmac_f32_e32 v36, v93, v101
	ds_read_b128 v[98:101], v63 offset:3328
	s_waitcnt lgkmcnt(2)
	v_fmac_f32_e32 v35, v86, v58
	v_fmac_f32_e32 v37, v90, v58
	v_fmac_f32_e32 v35, v87, v59
	v_fmac_f32_e32 v37, v91, v59
	v_fmac_f32_e32 v35, v88, v60
	v_fmac_f32_e32 v37, v92, v60
	v_fmac_f32_e32 v35, v89, v61
	v_fmac_f32_e32 v37, v93, v61
	ds_read_b128 v[58:61], v63 offset:3584
	s_waitcnt lgkmcnt(2)
	v_fmac_f32_e32 v30, v86, v94
	v_fmac_f32_e32 v32, v90, v94
	v_fmac_f32_e32 v30, v87, v95
	v_fmac_f32_e32 v32, v91, v95
	v_fmac_f32_e32 v30, v88, v96
	v_fmac_f32_e32 v32, v92, v96
	v_fmac_f32_e32 v30, v89, v97
	v_fmac_f32_e32 v32, v93, v97
	ds_read_b128 v[94:97], v63 offset:3840
	s_waitcnt lgkmcnt(2)
	v_fmac_f32_e32 v31, v86, v98
	v_fmac_f32_e32 v33, v90, v98
	v_fmac_f32_e32 v31, v87, v99
	v_fmac_f32_e32 v33, v91, v99
	v_fmac_f32_e32 v31, v88, v100
	v_fmac_f32_e32 v33, v92, v100
	v_fmac_f32_e32 v31, v89, v101
	v_fmac_f32_e32 v33, v93, v101
	s_waitcnt lgkmcnt(1)
	v_fmac_f32_e32 v26, v86, v58
	v_fmac_f32_e32 v28, v90, v58
	v_fmac_f32_e32 v26, v87, v59
	v_fmac_f32_e32 v28, v91, v59
	v_fmac_f32_e32 v26, v88, v60
	v_fmac_f32_e32 v28, v92, v60
	v_fmac_f32_e32 v26, v89, v61
	v_fmac_f32_e32 v28, v93, v61
	s_waitcnt lgkmcnt(0)
	v_fmac_f32_e32 v27, v86, v94
	v_fmac_f32_e32 v29, v90, v94
	v_fmac_f32_e32 v27, v87, v95
	v_fmac_f32_e32 v29, v91, v95
	v_fmac_f32_e32 v27, v88, v96
	v_fmac_f32_e32 v29, v92, v96
	v_fmac_f32_e32 v27, v89, v97
	v_fmac_f32_e32 v29, v93, v97
	s_add_i32 s100, s100, 1
	s_branch .Lhy_loop
;     ...
;         for (int k4 = 0; k4 < 16; ++k4) {
;             float wf[4], wb[4];
; #pragma unroll
;             for (int j = 0; j < 4; ++j) { wf[j] = w3[(k4 * 4 + j) * 1024 + tid]; wb[j] = w3[(k4 * 4 + j) * 1024 + 512 + tid]; }
; #pragma unroll
;             for (int pp = 0; pp < 16; ++pp) {
;                 const float4 hv = *(const float4*)&h2[(hp * 16 + pp) * 64 + k4 * 4];
;                 accf[pp] += hv.x * wf[0]; accf[pp] += hv.y * wf[1]; accf[pp] += hv.z * wf[2]; accf[pp] += hv.w * wf[3];
;                 accb[pp] += hv.x * wb[0]; accb[pp] += hv.y * wb[1]; accb[pp] += hv.z * wb[2]; accb[pp] += hv.w * wb[3];
;             }
;         }
; #pragma unroll
;         for (int pp = 0; pp < 16; ++pp) {
;             const int pos = p0 + hp * 16 + pp;
;             const float t = (float)pos / (float)(l - 1);
;             const float win = expf(-t * delta);
;             const float f = accf[pp] * win, b = accb[pp] * win;
;             HF[pos] = f; asum += fabsf(f);
;             if (pos >= 1) { HF[-pos] = b; asum += fabsf(b); }
.Lhy_last:
	v_mov_b32_e32 v63, s101
	s_add_i32 s101, s101, 16
	ds_read_b128 v[94:97], v63
	ds_read_b128 v[98:101], v63 offset:256
	s_waitcnt vmcnt(0)
	ds_read_b128 v[58:61], v63 offset:512
	s_waitcnt lgkmcnt(2)
	v_fmac_f32_e32 v54, v86, v94
	v_fmac_f32_e32 v56, v90, v94
	v_fmac_f32_e32 v54, v87, v95
	v_fmac_f32_e32 v56, v91, v95
	v_fmac_f32_e32 v54, v88, v96
	v_fmac_f32_e32 v56, v92, v96
	v_fmac_f32_e32 v54, v89, v97
	v_fmac_f32_e32 v56, v93, v97
	ds_read_b128 v[94:97], v63 offset:768
	s_waitcnt lgkmcnt(2)
	v_fmac_f32_e32 v55, v86, v98
	v_fmac_f32_e32 v57, v90, v98
	v_fmac_f32_e32 v55, v87, v99
	v_fmac_f32_e32 v57, v91, v99
	v_fmac_f32_e32 v55, v88, v100
	v_fmac_f32_e32 v57, v92, v100
	v_fmac_f32_e32 v55, v89, v101
	v_fmac_f32_e32 v57, v93, v101
	ds_read_b128 v[98:101], v63 offset:1024
	s_waitcnt lgkmcnt(2)
	v_fmac_f32_e32 v50, v86, v58
	v_fmac_f32_e32 v52, v90, v58
	v_fmac_f32_e32 v50, v87, v59
	v_fmac_f32_e32 v52, v91, v59
	v_fmac_f32_e32 v50, v88, v60
	v_fmac_f32_e32 v52, v92, v60
	v_fmac_f32_e32 v50, v89, v61
	v_fmac_f32_e32 v52, v93, v61
	ds_read_b128 v[58:61], v63 offset:1280
	s_waitcnt lgkmcnt(2)
	v_fmac_f32_e32 v51, v86, v94
	v_fmac_f32_e32 v53, v90, v94
	v_fmac_f32_e32 v51, v87, v95
	v_fmac_f32_e32 v53, v91, v95
	v_fmac_f32_e32 v51, v88, v96
	v_fmac_f32_e32 v53, v92, v96
	v_fmac_f32_e32 v51, v89, v97
	v_fmac_f32_e32 v53, v93, v97
	ds_read_b128 v[94:97], v63 offset:1536
	s_waitcnt lgkmcnt(2)
	v_fmac_f32_e32 v46, v86, v98
	v_fmac_f32_e32 v48, v90, v98
	v_fmac_f32_e32 v46, v87, v99
	v_fmac_f32_e32 v48, v91, v99
	v_fmac_f32_e32 v46, v88, v100
	v_fmac_f32_e32 v48, v92, v100
	v_fmac_f32_e32 v46, v89, v101
	v_fmac_f32_e32 v48, v93, v101
	ds_read_b128 v[98:101], v63 offset:1792
	s_waitcnt lgkmcnt(2)
	v_fmac_f32_e32 v47, v86, v58
	v_fmac_f32_e32 v49, v90, v58
	v_fmac_f32_e32 v47, v87, v59
	v_fmac_f32_e32 v49, v91, v59
	v_fmac_f32_e32 v47, v88, v60
	v_fmac_f32_e32 v49, v92, v60
	v_fmac_f32_e32 v47, v89, v61
	v_fmac_f32_e32 v49, v93, v61
	ds_read_b128 v[58:61], v63 offset:2048
	s_waitcnt lgkmcnt(2)
	v_fmac_f32_e32 v42, v86, v94
	v_fmac_f32_e32 v44, v90, v94
	v_fmac_f32_e32 v42, v87, v95
	v_fmac_f32_e32 v44, v91, v95
	v_fmac_f32_e32 v42, v88, v96
	v_fmac_f32_e32 v44, v92, v96
	v_fmac_f32_e32 v42, v89, v97
	v_fmac_f32_e32 v44, v93, v97
	ds_read_b128 v[94:97], v63 offset:2304
	s_waitcnt lgkmcnt(2)
	v_fmac_f32_e32 v43, v86, v98
	v_fmac_f32_e32 v45, v90, v98
	v_fmac_f32_e32 v43, v87, v99
	v_fmac_f32_e32 v45, v91, v99
	v_fmac_f32_e32 v43, v88, v100
	v_fmac_f32_e32 v45, v92, v100
	v_fmac_f32_e32 v43, v89, v101
	v_fmac_f32_e32 v45, v93, v101
	ds_read_b128 v[98:101], v63 offset:2560
	s_waitcnt lgkmcnt(2)
	v_fmac_f32_e32 v38, v86, v58
	v_fmac_f32_e32 v40, v90, v58
	v_fmac_f32_e32 v38, v87, v59
	v_fmac_f32_e32 v40, v91, v59
	v_fmac_f32_e32 v38, v88, v60
	v_fmac_f32_e32 v40, v92, v60
	v_fmac_f32_e32 v38, v89, v61
	v_fmac_f32_e32 v40, v93, v61
	ds_read_b128 v[58:61], v63 offset:2816
	s_waitcnt lgkmcnt(2)
	v_fmac_f32_e32 v39, v86, v94
	v_fmac_f32_e32 v41, v90, v94
	v_fmac_f32_e32 v39, v87, v95
	v_fmac_f32_e32 v41, v91, v95
	v_fmac_f32_e32 v39, v88, v96
	v_fmac_f32_e32 v41, v92, v96
	v_fmac_f32_e32 v39, v89, v97
	v_fmac_f32_e32 v41, v93, v97
	ds_read_b128 v[94:97], v63 offset:3072
	s_waitcnt lgkmcnt(2)
	v_fmac_f32_e32 v34, v86, v98
	v_fmac_f32_e32 v36, v90, v98
	v_fmac_f32_e32 v34, v87, v99
	v_fmac_f32_e32 v36, v91, v99
	v_fmac_f32_e32 v34, v88, v100
	v_fmac_f32_e32 v36, v92, v100
	v_fmac_f32_e32 v34, v89, v101
	v_fmac_f32_e32 v36, v93, v101
	ds_read_b128 v[98:101], v63 offset:3328
	s_waitcnt lgkmcnt(2)
	v_fmac_f32_e32 v35, v86, v58
	v_fmac_f32_e32 v37, v90, v58
	v_fmac_f32_e32 v35, v87, v59
	v_fmac_f32_e32 v37, v91, v59
	v_fmac_f32_e32 v35, v88, v60
	v_fmac_f32_e32 v37, v92, v60
	v_fmac_f32_e32 v35, v89, v61
	v_fmac_f32_e32 v37, v93, v61
	ds_read_b128 v[58:61], v63 offset:3584
	s_waitcnt lgkmcnt(2)
	v_fmac_f32_e32 v30, v86, v94
	v_fmac_f32_e32 v32, v90, v94
	v_fmac_f32_e32 v30, v87, v95
	v_fmac_f32_e32 v32, v91, v95
	v_fmac_f32_e32 v30, v88, v96
	v_fmac_f32_e32 v32, v92, v96
	v_fmac_f32_e32 v30, v89, v97
	v_fmac_f32_e32 v32, v93, v97
	ds_read_b128 v[94:97], v63 offset:3840
	s_waitcnt lgkmcnt(2)
	v_fmac_f32_e32 v31, v86, v98
	v_fmac_f32_e32 v33, v90, v98
	v_fmac_f32_e32 v31, v87, v99
	v_fmac_f32_e32 v33, v91, v99
	v_fmac_f32_e32 v31, v88, v100
	v_fmac_f32_e32 v33, v92, v100
	v_fmac_f32_e32 v31, v89, v101
	v_fmac_f32_e32 v33, v93, v101
	s_waitcnt lgkmcnt(1)
	v_fmac_f32_e32 v26, v86, v58
	v_fmac_f32_e32 v28, v90, v58
	v_fmac_f32_e32 v26, v87, v59
	v_fmac_f32_e32 v28, v91, v59
	v_fmac_f32_e32 v26, v88, v60
	v_fmac_f32_e32 v28, v92, v60
	v_fmac_f32_e32 v26, v89, v61
	v_fmac_f32_e32 v28, v93, v61
	s_waitcnt lgkmcnt(0)
	v_fmac_f32_e32 v27, v86, v94
	v_fmac_f32_e32 v29, v90, v94
	v_fmac_f32_e32 v27, v87, v95
	v_fmac_f32_e32 v29, v91, v95
	v_fmac_f32_e32 v27, v88, v96
	v_fmac_f32_e32 v29, v92, v96
	v_fmac_f32_e32 v27, v89, v97
	v_fmac_f32_e32 v29, v93, v97
	s_lshl_b32 s2, s7, 4
	s_or_b32 s2, s2, s15
	v_cvt_f32_i32_e32 v2, s2
	s_ashr_i32 s3, s2, 31
	s_cmp_gt_i32 s2, 0
	v_div_scale_f32 v3, s[4:5], v77, v77, -v2
	v_rcp_f32_e32 v4, v3
	v_div_scale_f32 v5, vcc, -v2, v77, -v2
	v_fma_f32 v58, -v3, v4, 1.0
	v_fmac_f32_e32 v4, v58, v4
	v_mul_f32_e32 v58, v5, v4
	v_fma_f32 v59, -v3, v58, v5
	v_fmac_f32_e32 v58, v59, v4
	v_fma_f32 v3, -v3, v58, v5
	v_div_fmas_f32 v3, v3, v4, v58
	v_div_fixup_f32 v2, v3, v77, -v2
	v_mul_f32_e64 v2, |v67|, v2
	v_mul_f32_e32 v3, 0x3fb8aa3b, v2
	v_fma_f32 v4, v2, s40, -v3
	v_rndne_f32_e32 v5, v3
	v_fmac_f32_e32 v4, 0x32a5705f, v2
	v_sub_f32_e32 v3, v3, v5
	v_add_f32_e32 v3, v3, v4
	v_cvt_i32_f32_e32 v4, v5
	v_exp_f32_e32 v3, v3
	v_cmp_ngt_f32_e32 vcc, s41, v2
	v_ldexp_f32 v3, v3, v4
	s_nop 0
	v_cndmask_b32_e32 v3, 0, v3, vcc
	v_cmp_nlt_f32_e32 vcc, s42, v2
	s_nop 1
	v_cndmask_b32_e32 v5, v76, v3, vcc
	v_mul_f32_e32 v4, v5, v54
	v_lshl_add_u64 v[2:3], s[2:3], 2, v[24:25]
	global_store_dword v[2:3], v4, off
	v_add_f32_e64 v4, v22, |v4|
	s_cbranch_scc0 .LBB0_79
	s_sub_i32 s4, 0, s2
	v_mul_f32_e32 v5, v5, v56
	s_ashr_i32 s5, s4, 31
	v_add_f32_e64 v4, |v5|, v4
	v_lshl_add_u64 v[58:59], s[4:5], 2, v[24:25]
	global_store_dword v[58:59], v5, off
